# speedup vs baseline: 1.0133x; 1.0133x over previous
.Llin_skip:
	s_mov_b64 exec, s[58:59]
	s_nop 4
	v_add_f32_dpp v40, v40, v40 quad_perm:[1,0,3,2] row_mask:0xf bank_mask:0xf
	v_add_f32_dpp v41, v41, v41 quad_perm:[1,0,3,2] row_mask:0xf bank_mask:0xf
	s_nop 1
	v_add_f32_dpp v40, v40, v40 quad_perm:[2,3,0,1] row_mask:0xf bank_mask:0xf
	v_add_f32_dpp v41, v41, v41 quad_perm:[2,3,0,1] row_mask:0xf bank_mask:0xf
	v_cmp_eq_u32_e32 vcc, 0, v99
	s_movk_i32 s45, 0xe0
	v_cmp_gt_u32_e64 s[60:61], s45, v98
	v_add_u32_e32 v12, 0x38000000, v101
	v_cvt_f32_u32_e32 v48, v96
	s_and_b64 vcc, vcc, s[60:61]
	s_and_saveexec_b64 s[60:61], vcc
	v_mov_b32_e32 v49, v100
	v_mul_f32_e32 v12, v12, v20
	v_mul_f32_e32 v46, v40, v100
	v_mul_f32_e32 v47, v41, v100
	v_mul_f32_e32 v48, v48, v100
	v_lshlrev_b32_e32 v13, 4, v98
	v_add_u32_e32 v13, 0x23360, v13
	ds_write_b128 v13, v[46:49]
	v_lshlrev_b32_e32 v13, 2, v98
	v_add_u32_e32 v13, 0x22200, v13
	ds_write_b32 v13, v12
	s_mov_b64 exec, s[60:61]
	s_waitcnt lgkmcnt(0)
	s_barrier
	v_mov_b32_e32 v11, 0x24860
	ds_read_b64 v[12:13], v11
	v_mov_b32_e32 v62, 0x23360
	v_mov_b32_e32 v2, v55
	s_waitcnt lgkmcnt(0)
	v_readfirstlane_b32 s62, v12
	v_readfirstlane_b32 s63, v13
	s_add_i32 s62, s62, 1
	s_lshr_b32 s62, s62, 1
	s_add_i32 s63, s63, 1
	s_lshr_b32 s63, s63, 1
	s_mov_b64 exec, 1
	ds_add_rtn_u32 v10, v59, v60
	s_mov_b64 exec, -1
	s_waitcnt lgkmcnt(0)
	s_branch .Lp_top

.Lp_top:
	s_setprio 2
	v_readfirstlane_b32 s34, v10
	s_cmp_lt_u32 s34, s62
	s_cselect_b32 s45, s64, s65
	s_cselect_b32 s46, 0, s62
	s_cselect_b32 s48, s62, s63
	s_sub_u32 s47, s34, s46
	s_cmp_ge_u32 s47, s48
	s_cbranch_scc1 .Lp_done
	s_lshl_b32 s47, s47, 3
	s_add_u32 s45, s45, s47
	v_mov_b32_e32 v11, s45
	ds_read2_b32 v[12:13], v11 offset1:1
	s_waitcnt lgkmcnt(0)
	v_readfirstlane_b32 s35, v12
	v_readfirstlane_b32 s36, v13
	s_nop 1
	v_mov_b32_e32 v10, s35
	v_mov_b32_e32 v11, s36
	v_cndmask_b32_e64 v12, v10, v11, s[54:55]
	v_cndmask_b32_e64 v13, v10, v11, s[56:57]
	v_lshl_add_u32 v12, v12, 3, v61
	v_lshl_add_u32 v14, v13, 4, v62
	ds_read_b64 v[2:3], v12
	ds_read_b128 v[4:7], v14
	v_mad_u32_u24 v9, v13, s49, v58
	v_mov_b32_e32 v8, v56
	s_waitcnt lgkmcnt(0)
	v_add_u32_e32 v2, v2, v55
	v_and_b32_e32 v3, v3, v63
	s_nop 0
	v_readlane_b32 s41, v3, 0
	v_readlane_b32 s42, v3, 4
	s_max_u32 s43, s41, s42
	s_cmp_eq_u32 s43, 0
	s_cbranch_scc1 .Lp_zero
	ds_read_b64 v[36:37], v2
	v_cmp_gt_u32_e32 vcc, v3, v8
	v_add_u32_e32 v2, 64, v2
	v_add_u32_e32 v8, 16, v8
	v_mov_b32_e32 v33, 0x3c00
	s_waitcnt lgkmcnt(0)
	v_perm_b32 v32, v37, v36, v57
	v_cndmask_b32_e32 v33, 0, v33, vcc
	s_nop 0
	v_cndmask_b32_e32 v32, 0, v32, vcc
	s_nop 1
	v_mfma_f32_32x32x16_f16 v[96:111], v[32:35], v[64:67], 0
	v_mfma_f32_32x32x16_f16 v[112:127], v[32:35], v[68:71], 0
	s_setprio 0
	s_nop 10
	s_mov_b32 s45, s43
	s_min_u32 s46, s45, 16
	s_cmp_eq_u32 s46, 16
	s_cbranch_scc1 .Lf16
	s_cmp_eq_u32 s46, 15
	s_cbranch_scc1 .Lf15
	s_cmp_eq_u32 s46, 14
	s_cbranch_scc1 .Lf14
	s_cmp_eq_u32 s46, 13
	s_cbranch_scc1 .Lf13
	s_cmp_eq_u32 s46, 12
	s_cbranch_scc1 .Lf12
	s_cmp_eq_u32 s46, 11
	s_cbranch_scc1 .Lf11
	s_cmp_eq_u32 s46, 10
	s_cbranch_scc1 .Lf10
	s_cmp_eq_u32 s46, 9
	s_cbranch_scc1 .Lf9
	s_cmp_eq_u32 s46, 8
	s_cbranch_scc1 .Lf8
	s_cmp_eq_u32 s46, 7
	s_cbranch_scc1 .Lf7
	s_cmp_eq_u32 s46, 6
	s_cbranch_scc1 .Lf6
	s_cmp_eq_u32 s46, 5
	s_cbranch_scc1 .Lf5
	s_cmp_eq_u32 s46, 4
	s_cbranch_scc1 .Lf4
	s_cmp_eq_u32 s46, 3
	s_cbranch_scc1 .Lf3
	s_cmp_eq_u32 s46, 2
	s_cbranch_scc1 .Lf2

.Lp_fin:
	s_setprio 2
	s_mov_b64 exec, 1
	ds_add_rtn_u32 v10, v59, v60
	s_mov_b64 exec, -1
	v_mul_f32_e32 v40, v7, v24
	v_fma_mix_f32 v40, v6, v65, v40 op_sel_hi:[0,1,0]
	v_fma_mix_f32 v40, v5, v64, v40 op_sel:[0,1,0] op_sel_hi:[0,1,0]
	v_fma_mixlo_f16 v40, v4, v64, v40 op_sel_hi:[0,1,0]
	ds_write_b16 v9, v40 offset:0
	v_mul_f32_e32 v41, v7, v25
	v_fma_mix_f32 v41, v6, v69, v41 op_sel_hi:[0,1,0]
	v_fma_mix_f32 v41, v5, v68, v41 op_sel:[0,1,0] op_sel_hi:[0,1,0]
	v_fma_mixlo_f16 v41, v4, v68, v41 op_sel_hi:[0,1,0]
	ds_write_b16 v9, v41 offset:64
	v_mul_f32_e32 v40, v7, v26
	v_fma_mix_f32 v40, v6, v73, v40 op_sel_hi:[0,1,0]
	v_fma_mix_f32 v40, v5, v72, v40 op_sel:[0,1,0] op_sel_hi:[0,1,0]
	v_fma_mixlo_f16 v40, v4, v72, v40 op_sel_hi:[0,1,0]
	ds_write_b16 v9, v40 offset:128
	v_mul_f32_e32 v41, v7, v27
	v_fma_mix_f32 v41, v6, v77, v41 op_sel_hi:[0,1,0]
	v_fma_mix_f32 v41, v5, v76, v41 op_sel:[0,1,0] op_sel_hi:[0,1,0]
	v_fma_mixlo_f16 v41, v4, v76, v41 op_sel_hi:[0,1,0]
	ds_write_b16 v9, v41 offset:192
	v_mul_f32_e32 v40, v7, v28
	v_fma_mix_f32 v40, v6, v81, v40 op_sel_hi:[0,1,0]
	v_fma_mix_f32 v40, v5, v80, v40 op_sel:[0,1,0] op_sel_hi:[0,1,0]
	v_fma_mixlo_f16 v40, v4, v80, v40 op_sel_hi:[0,1,0]
	ds_write_b16 v9, v40 offset:256
	v_mul_f32_e32 v41, v7, v29
	v_fma_mix_f32 v41, v6, v85, v41 op_sel_hi:[0,1,0]
	v_fma_mix_f32 v41, v5, v84, v41 op_sel:[0,1,0] op_sel_hi:[0,1,0]
	v_fma_mixlo_f16 v41, v4, v84, v41 op_sel_hi:[0,1,0]
	ds_write_b16 v9, v41 offset:320
	v_mul_f32_e32 v40, v7, v30
	v_fma_mix_f32 v40, v6, v89, v40 op_sel_hi:[0,1,0]
	v_fma_mix_f32 v40, v5, v88, v40 op_sel:[0,1,0] op_sel_hi:[0,1,0]
	v_fma_mixlo_f16 v40, v4, v88, v40 op_sel_hi:[0,1,0]
	ds_write_b16 v9, v40 offset:384
	v_mul_f32_e32 v41, v7, v31
	v_fma_mix_f32 v41, v6, v93, v41 op_sel_hi:[0,1,0]
	v_fma_mix_f32 v41, v5, v92, v41 op_sel:[0,1,0] op_sel_hi:[0,1,0]
	v_fma_mixlo_f16 v41, v4, v92, v41 op_sel_hi:[0,1,0]
	ds_write_b16 v9, v41 offset:448
	s_branch .Lp_next
